# baseline (speedup 1.0000x reference)
_Z6k_prepPKiPKfPiS3_P15HIP_vector_typeIjLj4EEPh:
	s_mov_b64 s[4:5], -1
	s_cmpk_lt_i32 s2, 10
	v_lshl_or_b32 v2, s2, 9, v0
	s_cbranch_scc0 .LBB0_20
	v_mov_b32_e32 v3, v2
	s_movk_i32 s3, 0x1300
	v_cmp_gt_i32_e32 vcc, s3, v3
	s_and_saveexec_b64 s[4:5], vcc
	s_cbranch_execz .LBB0_19
	s_load_dwordx2 s[6:7], s[0:1], 0x8
	s_load_dwordx2 s[8:9], s[0:1], 0x20
	v_bfe_u32 v1, v0, 6, 2
	v_and_b32_e32 v4, 15, v0
	v_lshl_or_b32 v4, v1, 4, v4
	v_lshrrev_b32_e32 v5, 1, v0
	v_lshrrev_b32_e32 v3, 8, v3
	v_and_b32_e32 v5, 24, v5
	v_mul_u32_u24_e32 v4, 0x4b0, v4
	v_lshl_or_b32 v8, v3, 5, v5
	v_lshlrev_b32_e32 v4, 2, v4
	v_mov_b32_e32 v5, 0
	s_movk_i32 s3, 0x258
	v_mov_b32_e32 v9, 0
	v_mov_b32_e32 v12, 0
	v_mov_b32_e32 v13, 0
	v_mov_b32_e32 v14, 0
	v_mov_b32_e32 v15, 0
	v_mov_b32_e32 v16, 0
	v_mov_b32_e32 v17, 0
	v_mov_b32_e32 v18, 0
	v_mov_b32_e32 v19, 0
	v_mov_b32_e32 v20, 0
	v_mov_b32_e32 v21, 0
	v_mov_b32_e32 v22, 0
	v_mov_b32_e32 v23, 0
	v_mov_b32_e32 v24, 0
	v_mov_b32_e32 v25, 0
	v_mov_b32_e32 v26, 0
	v_mov_b32_e32 v27, 0
	s_waitcnt lgkmcnt(0)
	v_lshl_add_u64 v[6:7], s[6:7], 0, v[4:5]
	v_cmp_gt_u32_e32 vcc, s3, v8
	v_lshlrev_b32_e32 v8, 3, v8
	v_lshl_add_u64 v[10:11], v[6:7], 0, v[8:9]
	s_and_saveexec_b64 s[6:7], vcc
	global_load_dwordx4 v[12:15], v[10:11], off
	global_load_dwordx4 v[16:19], v[10:11], off offset:16
	global_load_dwordx4 v[20:23], v[10:11], off offset:32
	global_load_dwordx4 v[24:27], v[10:11], off offset:48
	s_or_b64 exec, exec, s[6:7]
	v_and_b32_e32 v4, 63, v0
	v_lshlrev_b32_e32 v3, 9, v3
	v_lshlrev_b32_e32 v1, 6, v1
	v_or3_b32 v4, v3, v1, v4
	v_mov_b32_e32 v5, 0
	v_lshl_add_u64 v[10:11], v[4:5], 4, s[8:9]
	v_add_u32_e32 v4, 0x100, v4
	v_lshl_add_u64 v[4:5], v[4:5], 4, s[8:9]
	s_waitcnt vmcnt(0)
	v_cvt_pk_f16_f32 v28, v12, v14
	v_cvt_pk_f16_f32 v29, v16, v18
	v_cvt_pk_f16_f32 v30, v20, v22
	v_cvt_pk_f16_f32 v31, v24, v26
	v_cvt_pk_f16_f32 v32, v13, v15
	v_cvt_pk_f16_f32 v33, v17, v19
	v_cvt_pk_f16_f32 v34, v21, v23
	v_cvt_pk_f16_f32 v35, v25, v27
	global_store_dwordx4 v[10:11], v[28:31], off sc0 sc1
	global_store_dwordx4 v[4:5], v[32:35], off sc0 sc1

.LBB0_20:
	s_andn2_b64 vcc, exec, s[4:5]
	s_cbranch_vccnz .LBB0_27
	s_load_dwordx2 s[4:5], s[0:1], 0x0
	s_load_dwordx2 s[6:7], s[0:1], 0x18
	s_sub_u32 s2, s2, 10
	v_lshl_or_b32 v2, s2, 9, v0
	v_lshl_add_u32 v4, v0, 8, s2
	v_ashrrev_i32_e32 v5, 31, v4
	v_ashrrev_i32_e32 v3, 31, v2
	s_waitcnt lgkmcnt(0)
	v_lshl_add_u64 v[4:5], v[4:5], 2, s[4:5]
	global_load_dword v4, v[4:5], off
	v_and_b32_e32 v1, 63, v0
	v_lshl_add_u64 v[2:3], v[2:3], 2, s[6:7]
	v_cmp_eq_u32_e64 s[4:5], 0, v1
	s_waitcnt vmcnt(0)
	v_cmp_ne_u32_e32 vcc, 1, v4
	global_store_dword v[2:3], v4, off sc0 sc1
	s_and_saveexec_b64 s[6:7], s[4:5]
	s_bcnt1_i32_b64 s3, vcc
	v_lshrrev_b32_e32 v1, 4, v0
	v_mov_b32_e32 v2, s3
	ds_write_b32 v1, v2
	s_or_b64 exec, exec, s[6:7]
	v_mov_b32_e32 v1, 0
	s_waitcnt lgkmcnt(0)
	s_barrier
	ds_read_b128 v[6:9], v1
	ds_read_b128 v[10:13], v1 offset:16
	v_cmp_eq_u32_e32 vcc, 0, v0
	s_waitcnt lgkmcnt(1)
	v_add_u32_e32 v2, v7, v6
	v_add_u32_e32 v2, v8, v2
	v_add_u32_e32 v2, v9, v2
	s_waitcnt lgkmcnt(0)
	v_add_u32_e32 v2, v10, v2
	v_add_u32_e32 v2, v11, v2
	v_add_u32_e32 v2, v12, v2
	v_add_u32_e32 v2, v13, v2
	s_and_saveexec_b64 s[4:5], vcc
	s_cbranch_execz .LBB0_25
	s_load_dwordx2 s[6:7], s[0:1], 0x10
	s_ashr_i32 s3, s2, 31
	s_lshl_b64 s[2:3], s[2:3], 2
	s_waitcnt lgkmcnt(0)
	s_add_u32 s2, s6, s2
	s_addc_u32 s3, s7, s3
	global_store_dword v1, v2, s[2:3] sc0 sc1
